# speedup vs baseline: 1.0095x; 1.0095x over previous
_Z8knn_gemmPKcS0_Pi:
	s_ashr_i32 s3, s2, 31
	s_lshr_b32 s3, s3, 29
	s_add_i32 s3, s2, s3
	s_ashr_i32 s4, s3, 3
	s_and_b32 s3, s3, -8
	s_sub_i32 s3, s2, s3
	s_cmp_lt_i32 s3, 0
	s_movk_i32 s12, 0x188
	s_cselect_b32 s5, s12, 0x187
	s_mul_i32 s3, s5, s3
	s_add_i32 s3, s3, s4
	s_ashr_i32 s4, s3, 31
	s_lshr_b32 s4, s4, 27
	s_add_i32 s10, s3, s4
	s_ashr_i32 s4, s10, 5
	s_lshl_b32 s11, s4, 2
	s_sub_i32 s4, 0x187, s11
	s_min_i32 s13, s4, 4
	s_abs_i32 s14, s13
	v_cvt_f32_u32_e32 v1, s14
	s_andn2_b32 s10, s10, 31
	s_load_dwordx4 s[4:7], s[0:1], 0x0
	s_load_dwordx2 s[8:9], s[0:1], 0x10
	s_sub_i32 s0, s3, s10
	v_rcp_iflag_f32_e32 v1, v1
	s_sub_i32 s10, 0, s14
	s_abs_i32 s3, s0
	s_xor_b32 s1, s0, s13
	v_mul_f32_e32 v1, 0x4f7ffffe, v1
	v_cvt_u32_f32_e32 v1, v1
	s_ashr_i32 s1, s1, 31
	v_lshrrev_b32_e32 v2, 8, v0
	v_lshlrev_b32_e32 v168, 4, v0
	v_readfirstlane_b32 s15, v1
	s_mul_i32 s10, s10, s15
	s_mul_hi_u32 s10, s15, s10
	s_add_i32 s15, s15, s10
	s_mul_hi_u32 s10, s3, s15
	s_mul_i32 s15, s10, s14
	s_sub_i32 s3, s3, s15
	s_add_i32 s15, s10, 1
	s_sub_i32 s16, s3, s14
	s_cmp_ge_u32 s3, s14
	s_cselect_b32 s10, s15, s10
	s_cselect_b32 s3, s16, s3
	s_add_i32 s15, s10, 1
	s_cmp_ge_u32 s3, s14
	s_cselect_b32 s3, s15, s10
	s_xor_b32 s3, s3, s1
	s_sub_i32 s34, s3, s1
	s_mul_i32 s1, s34, s13
	s_sub_i32 s0, s0, s1
	s_add_i32 s11, s11, s0
	v_readfirstlane_b32 s1, v0
	s_sub_i32 s13, 0x186, s11
	s_lshl_b32 s3, s1, 4
	s_mul_i32 s10, s34, 0x30000
	s_mul_hi_i32 s1, s34, 0x30000
	s_waitcnt lgkmcnt(0)
	s_add_u32 s10, s6, s10
	s_addc_u32 s11, s7, s1
	s_mul_i32 s14, s13, 0x30000
	s_mul_hi_i32 s1, s13, 0x30000
	s_add_u32 s22, s4, s14
	v_readfirstlane_b32 s0, v2
	s_addc_u32 s23, s5, s1
	s_cmp_eq_u32 s0, 0
	s_cselect_b64 s[0:1], -1, 0
	s_add_u32 s16, s10, 0x2000
	s_addc_u32 s17, s11, 0
	s_add_u32 s18, s22, 0xfffff000
	s_addc_u32 s19, s23, -1
	s_and_b64 s[14:15], s[0:1], exec
	s_cselect_b32 s17, s17, s19
	s_cselect_b32 s16, s16, s18
	s_add_u32 s18, s22, 0x1000
	s_addc_u32 s19, s23, 0
	s_add_i32 s14, s3, 0
	s_mov_b64 s[20:21], s[10:11]
	s_add_i32 s15, s14, 0x2000
	v_lshrrev_b32_e32 v5, 2, v0
	v_lshrrev_b32_e32 v1, 4, v0
	s_add_i32 s16, s14, 0x4000
	v_and_b32_e32 v5, 2, v5
	s_add_u32 s18, s10, 0x3000
	s_addc_u32 s19, s11, 0
	s_add_u32 s3, s10, 0x5000
	s_addc_u32 s17, s11, 0
	s_add_u32 s20, s22, 0x2000
	s_addc_u32 s21, s23, 0
	s_and_b64 s[10:11], s[0:1], exec
	s_cselect_b32 s11, s17, s21
	s_cselect_b32 s10, s3, s20
	s_add_u32 s20, s22, 0x4000
	s_addc_u32 s21, s23, 0
	s_add_i32 s17, s14, 0x6000
	v_add_lshl_u32 v1, v5, v1, 3
	s_add_i32 s18, s14, 0x8000
	s_add_i32 s19, s14, 0xa000
	v_and_b32_e32 v3, 15, v0
	v_and_b32_e32 v5, 24, v1
	v_lshrrev_b32_e32 v1, 1, v0
	s_movk_i32 s3, 0x60
	s_add_i32 s20, s14, 0xc000
	v_and_or_b32 v1, v1, s3, v3
	v_lshl_or_b32 v2, v2, 6, v3
	s_add_u32 s21, s4, 0x12000
	v_and_b32_e32 v4, 48, v0
	v_mad_u32_u24 v6, v1, s3, 0
	v_mad_u32_u24 v2, v2, s3, 0
	s_addc_u32 s22, s5, 0
	v_add_u32_e32 v1, v6, v4
	v_add_u32_e32 v170, v2, v4
	v_add_u32_e32 v172, v6, v5
	v_add_u32_e32 v173, v2, v5
	v_mov_b32_e32 v39, 0
	s_add_u32 s23, s6, 0x12000
	v_add_u32_e32 v171, 0x3000, v170
	v_add_u32_e32 v174, 0x3040, v173
	v_mov_b32_e32 v169, v39
	v_add_u32_e32 v175, 0x12000, v1
	v_add_u32_e32 v176, 0x12040, v172
	v_add_u32_e32 v177, 0x15000, v170
	v_add_u32_e32 v178, 0x15040, v173
	v_add_u32_e32 v179, 0x12600, v1
	v_add_u32_e32 v180, 0x12640, v172
	v_add_u32_e32 v181, 0x15600, v170
	v_add_u32_e32 v182, 0x15640, v173
	v_add_u32_e32 v183, 0x15c00, v170
	v_add_u32_e32 v184, 0x15c40, v173
	v_add_u32_e32 v185, 0x16200, v170
	v_add_u32_e32 v186, 0x16240, v173
	s_addc_u32 s24, s7, 0
	v_mov_b32_e32 v187, 0x7f7f7f7f
	s_add_i32 s25, 0, 0x18000
	s_movk_i32 s26, 0xff80
	s_movk_i32 s27, 0x30e
	s_add_i32 s28, s14, 0xe000
	s_add_i32 s29, s20, 0x4000
	s_add_i32 s30, s14, 0x12000
	s_add_i32 s31, s14, 0x14000
	s_add_i32 s33, s14, 0x16000
	s_lshr_b32 s66, s14, 12
	s_and_b32 s54, s14, 0xfff
	s_mul_i32 s67, s66, 0x6000
	s_add_i32 s54, s54, s67
	s_add_i32 s55, s54, 0x1000
	s_add_i32 s56, s54, 0x2000
	s_add_i32 s57, s54, 0x3000
	s_add_i32 s58, s54, 0x4000
	s_add_i32 s59, s54, 0x5000
	s_add_i32 s60, s54, 0xc000
	s_add_i32 s61, s54, 0xd000
	s_add_i32 s62, s54, 0xe000
	s_add_i32 s63, s54, 0xf000
	s_add_i32 s64, s54, 0x10000
	s_add_i32 s65, s54, 0x11000
	v_and_b32_e32 v228, 0x3ff, v168
	s_lshr_b32 s74, s14, 11
	s_and_b32 s74, s74, 1
	s_lshr_b32 s75, s14, 10
	s_and_b32 s75, s75, 1
	s_mul_i32 s75, s75, 0x1800
	s_add_i32 s75, s75, 0xc00
	s_lshr_b32 s76, s14, 10
	s_and_b32 s76, s76, 3
	s_mul_i32 s76, s76, 0x1800
	s_add_i32 s76, s76, 0xc00
	s_mul_i32 s67, s66, 0x6000
	s_add_i32 s76, s76, s67
	s_add_i32 s77, s76, 0xc000
	v_add_u32_e32 v229, 0x1000, v228
	v_add_u32_e32 v230, 0x2000, v228
	s_mul_i32 s68, s34, 0x30000
	s_mul_hi_i32 s69, s34, 0x30000
	s_add_u32 s68, s6, s68
	s_addc_u32 s69, s7, s69
	s_mul_i32 s70, s13, 0x30000
	s_mul_hi_i32 s71, s13, 0x30000
	s_add_u32 s70, s4, s70
	s_addc_u32 s71, s5, s71
	s_mul_i32 s67, s66, 0x3000
	s_add_u32 s68, s68, s67
	s_addc_u32 s69, s69, 0
	s_add_u32 s70, s70, s67
	s_addc_u32 s71, s71, 0
	s_cmp_eq_u32 s74, 1
	s_cselect_b32 s68, s70, s68
	s_cselect_b32 s69, s71, s69
	s_add_u32 s68, s68, s75
	s_addc_u32 s69, s69, 0
	s_mov_b32 m0, s76
	s_nop 0
	global_load_lds_dwordx4 v228, s[68:69] offset:-3072
	global_load_lds_dwordx4 v228, s[68:69] offset:-2048
	global_load_lds_dwordx4 v228, s[68:69] offset:-1024
	global_load_lds_dwordx4 v228, s[68:69]
	global_load_lds_dwordx4 v228, s[68:69] offset:1024
	global_load_lds_dwordx4 v228, s[68:69] offset:2048
	s_waitcnt vmcnt(0)
	s_barrier
	s_add_u32 s68, s68, 0x6000
	s_addc_u32 s69, s69, 0
	s_add_u32 s70, s70, 0x6000
	s_addc_u32 s71, s71, 0
	s_mov_b32 m0, s77
	s_nop 0
	global_load_lds_dwordx4 v228, s[68:69] offset:-3072
	global_load_lds_dwordx4 v228, s[68:69] offset:-2048
	global_load_lds_dwordx4 v228, s[68:69] offset:-1024
	global_load_lds_dwordx4 v228, s[68:69]
	global_load_lds_dwordx4 v228, s[68:69] offset:1024
	global_load_lds_dwordx4 v228, s[68:69] offset:2048
	ds_read_b128 v[2:5], v170 offset:12288
	ds_read_b64 v[6:7], v173 offset:12352
	ds_read_b128 v[8:11], v170 offset:13824
	ds_read_b64 v[12:13], v173 offset:13888
	ds_read_b128 v[14:17], v170 offset:15360
	ds_read_b64 v[18:19], v173 offset:15424
	ds_read_b128 v[26:29], v170 offset:16896
	ds_read_b64 v[30:31], v173 offset:16960
	ds_read_b128 v[20:23], v1
	ds_read_b64 v[24:25], v172 offset:64
	ds_read_b128 v[32:35], v1 offset:1536
	ds_read_b64 v[36:37], v172 offset:1600
	s_branch .LBB1_2
.LBB1_1:
	v_mov_b32_e32 v215, 0
	v_and_b32_e32 v194, 0xffffff80, v164
	v_and_or_b32 v195, v165, s26, 1
	v_max_i32_e32 v196, v194, v195
	v_min_i32_e32 v197, v194, v195
	v_and_or_b32 v198, v166, s26, 2
	v_max_i32_e32 v196, v196, v198
	v_med3_i32 v194, v194, v195, v198
	v_min_i32_e32 v195, v197, v198
	v_and_or_b32 v197, v167, s26, 3
	v_max_i32_e32 v198, v196, v197
	v_med3_i32 v196, v196, v194, v197
	v_min_i32_e32 v194, v194, v197
	v_max_i32_e32 v194, v195, v194
	v_and_or_b32 v195, v160, s26, 4
	v_max_i32_e32 v197, v198, v195
	v_med3_i32 v198, v198, v196, v195
	v_med3_i32 v194, v196, v194, v195
	v_and_or_b32 v195, v161, s26, 5
	v_max_i32_e32 v196, v197, v195
	v_med3_i32 v197, v197, v198, v195
	v_med3_i32 v194, v198, v194, v195
	v_and_or_b32 v195, v162, s26, 6
	v_max_i32_e32 v198, v196, v195
	v_med3_i32 v196, v196, v197, v195
	v_med3_i32 v194, v197, v194, v195
	v_and_or_b32 v195, v163, s26, 7
	v_max_i32_e32 v197, v198, v195
	v_med3_i32 v198, v198, v196, v195
	v_med3_i32 v194, v196, v194, v195
	v_and_or_b32 v195, v156, s26, 8
	v_max_i32_e32 v196, v197, v195
	v_med3_i32 v197, v197, v198, v195
	v_med3_i32 v194, v198, v194, v195
	v_and_or_b32 v195, v157, s26, 9
	v_max_i32_e32 v198, v196, v195
	v_med3_i32 v196, v196, v197, v195
	v_med3_i32 v194, v197, v194, v195
	v_and_or_b32 v195, v158, s26, 10
	v_max_i32_e32 v197, v198, v195
	v_med3_i32 v198, v198, v196, v195
	v_med3_i32 v194, v196, v194, v195
	v_and_or_b32 v195, v159, s26, 11
	v_max_i32_e32 v196, v197, v195
	v_med3_i32 v197, v197, v198, v195
	v_med3_i32 v194, v198, v194, v195
	v_and_or_b32 v195, v152, s26, 12
	v_max_i32_e32 v198, v196, v195
	v_med3_i32 v196, v196, v197, v195
	v_med3_i32 v194, v197, v194, v195
	v_and_or_b32 v195, v153, s26, 13
	v_max_i32_e32 v197, v198, v195
	v_med3_i32 v198, v198, v196, v195
	v_med3_i32 v194, v196, v194, v195
	v_and_or_b32 v195, v154, s26, 14
	v_max_i32_e32 v196, v197, v195
	v_med3_i32 v197, v197, v198, v195
	v_med3_i32 v194, v198, v194, v195
	v_and_or_b32 v195, v155, s26, 15
	v_max_i32_e32 v198, v196, v195
	v_med3_i32 v196, v196, v197, v195
	v_med3_i32 v194, v197, v194, v195
	v_and_or_b32 v195, v144, s26, 16
	v_max_i32_e32 v197, v198, v195
	v_med3_i32 v198, v198, v196, v195
	v_med3_i32 v194, v196, v194, v195
	v_and_or_b32 v195, v145, s26, 17
	v_max_i32_e32 v196, v197, v195
	v_med3_i32 v197, v197, v198, v195
	v_med3_i32 v194, v198, v194, v195
	v_and_or_b32 v195, v146, s26, 18
	v_max_i32_e32 v198, v196, v195
	v_med3_i32 v196, v196, v197, v195
	v_med3_i32 v194, v197, v194, v195
	v_and_or_b32 v195, v147, s26, 19
	v_max_i32_e32 v197, v198, v195
	v_med3_i32 v198, v198, v196, v195
	v_med3_i32 v194, v196, v194, v195
	v_and_or_b32 v195, v136, s26, 20
	v_max_i32_e32 v196, v197, v195
	v_med3_i32 v197, v197, v198, v195
	v_med3_i32 v194, v198, v194, v195
	v_and_or_b32 v195, v137, s26, 21
	v_max_i32_e32 v198, v196, v195
	v_med3_i32 v196, v196, v197, v195
	v_med3_i32 v194, v197, v194, v195
	v_and_or_b32 v195, v138, s26, 22
	v_max_i32_e32 v197, v198, v195
	v_med3_i32 v198, v198, v196, v195
	v_med3_i32 v194, v196, v194, v195
	v_and_or_b32 v195, v139, s26, 23
	v_max_i32_e32 v196, v197, v195
	v_med3_i32 v197, v197, v198, v195
	v_med3_i32 v194, v198, v194, v195
	v_and_or_b32 v195, v128, s26, 24
	v_max_i32_e32 v198, v196, v195
	v_med3_i32 v196, v196, v197, v195
	v_med3_i32 v194, v197, v194, v195
	v_and_or_b32 v195, v129, s26, 25
	v_max_i32_e32 v197, v198, v195
	v_med3_i32 v198, v198, v196, v195
	v_med3_i32 v194, v196, v194, v195
	v_and_or_b32 v195, v130, s26, 26
	v_max_i32_e32 v196, v197, v195
	v_med3_i32 v197, v197, v198, v195
	v_med3_i32 v194, v198, v194, v195
	v_and_or_b32 v195, v131, s26, 27
	v_max_i32_e32 v198, v196, v195
	v_med3_i32 v196, v196, v197, v195
	v_med3_i32 v194, v197, v194, v195
	v_and_or_b32 v195, v120, s26, 28
	v_max_i32_e32 v197, v198, v195
	v_med3_i32 v198, v198, v196, v195
	v_med3_i32 v194, v196, v194, v195
	v_and_or_b32 v195, v121, s26, 29
	v_mov_b32_e32 v188, v0
	v_max_i32_e32 v196, v197, v195
	v_med3_i32 v197, v197, v198, v195
	v_med3_i32 v194, v198, v194, v195
	v_and_or_b32 v195, v122, s26, 30
	v_max_i32_e32 v198, v196, v195
	v_bfe_u32 v190, v188, 4, 2
	v_med3_i32 v196, v196, v197, v195
	v_med3_i32 v194, v197, v194, v195
	v_and_or_b32 v195, v123, s26, 31
	v_lshlrev_b32_e32 v193, 5, v190
	v_med3_i32 v194, v196, v194, v195
	v_max_i32_e32 v197, v198, v195
	v_med3_i32 v198, v198, v196, v195
	v_or_b32_e32 v214, v194, v193
	v_and_b32_e32 v194, 0xffffff80, v148
	v_and_or_b32 v195, v149, s26, 1
	v_or_b32_e32 v212, v197, v193
	v_or_b32_e32 v213, v198, v193
	v_max_i32_e32 v196, v194, v195
	v_min_i32_e32 v197, v194, v195
	v_and_or_b32 v198, v150, s26, 2
	v_max_i32_e32 v196, v196, v198
	v_med3_i32 v194, v194, v195, v198
	v_min_i32_e32 v195, v197, v198
	v_and_or_b32 v197, v151, s26, 3
	v_max_i32_e32 v198, v196, v197
	v_med3_i32 v196, v196, v194, v197
	v_min_i32_e32 v194, v194, v197
	v_max_i32_e32 v194, v195, v194
	v_and_or_b32 v195, v140, s26, 4
	v_max_i32_e32 v197, v198, v195
	v_med3_i32 v198, v198, v196, v195
	v_med3_i32 v194, v196, v194, v195
	v_and_or_b32 v195, v141, s26, 5
	v_max_i32_e32 v196, v197, v195
	v_med3_i32 v197, v197, v198, v195
	v_med3_i32 v194, v198, v194, v195
	v_and_or_b32 v195, v142, s26, 6
	v_max_i32_e32 v198, v196, v195
	v_med3_i32 v196, v196, v197, v195
	v_med3_i32 v194, v197, v194, v195
	v_and_or_b32 v195, v143, s26, 7
	v_max_i32_e32 v197, v198, v195
	v_med3_i32 v198, v198, v196, v195
	v_med3_i32 v194, v196, v194, v195
	v_and_or_b32 v195, v132, s26, 8
	v_max_i32_e32 v196, v197, v195
	v_med3_i32 v197, v197, v198, v195
	v_med3_i32 v194, v198, v194, v195
	v_and_or_b32 v195, v133, s26, 9
	v_max_i32_e32 v198, v196, v195
	v_med3_i32 v196, v196, v197, v195
	v_med3_i32 v194, v197, v194, v195
	v_and_or_b32 v195, v134, s26, 10
	v_max_i32_e32 v197, v198, v195
	v_med3_i32 v198, v198, v196, v195
	v_med3_i32 v194, v196, v194, v195
	v_and_or_b32 v195, v135, s26, 11
	v_max_i32_e32 v196, v197, v195
	v_med3_i32 v197, v197, v198, v195
	v_med3_i32 v194, v198, v194, v195
	v_and_or_b32 v195, v124, s26, 12
	v_max_i32_e32 v198, v196, v195
	v_med3_i32 v196, v196, v197, v195
	v_med3_i32 v194, v197, v194, v195
	v_and_or_b32 v195, v125, s26, 13
	v_max_i32_e32 v197, v198, v195
	v_med3_i32 v198, v198, v196, v195
	v_med3_i32 v194, v196, v194, v195
	v_and_or_b32 v195, v126, s26, 14
	v_max_i32_e32 v196, v197, v195
	v_med3_i32 v197, v197, v198, v195
	v_med3_i32 v194, v198, v194, v195
	v_and_or_b32 v195, v127, s26, 15
	v_max_i32_e32 v198, v196, v195
	v_med3_i32 v196, v196, v197, v195
	v_med3_i32 v194, v197, v194, v195
	v_and_or_b32 v195, v116, s26, 16
	v_max_i32_e32 v197, v198, v195
	v_med3_i32 v198, v198, v196, v195
	v_med3_i32 v194, v196, v194, v195
	v_and_or_b32 v195, v117, s26, 17
	v_max_i32_e32 v196, v197, v195
	v_med3_i32 v197, v197, v198, v195
	v_med3_i32 v194, v198, v194, v195
	v_and_or_b32 v195, v118, s26, 18
	v_max_i32_e32 v198, v196, v195
	v_med3_i32 v196, v196, v197, v195
	v_med3_i32 v194, v197, v194, v195
	v_and_or_b32 v195, v119, s26, 19
	v_max_i32_e32 v197, v198, v195
	v_med3_i32 v198, v198, v196, v195
	v_med3_i32 v194, v196, v194, v195
	v_and_or_b32 v195, v108, s26, 20
	v_max_i32_e32 v196, v197, v195
	v_med3_i32 v197, v197, v198, v195
	v_med3_i32 v194, v198, v194, v195
	v_and_or_b32 v195, v109, s26, 21
	v_max_i32_e32 v198, v196, v195
	v_med3_i32 v196, v196, v197, v195
	v_med3_i32 v194, v197, v194, v195
	v_and_or_b32 v195, v110, s26, 22
	v_max_i32_e32 v197, v198, v195
	v_med3_i32 v198, v198, v196, v195
	v_med3_i32 v194, v196, v194, v195
	v_and_or_b32 v195, v111, s26, 23
	v_max_i32_e32 v196, v197, v195
	v_med3_i32 v197, v197, v198, v195
	v_med3_i32 v194, v198, v194, v195
	v_and_or_b32 v195, v104, s26, 24
	v_max_i32_e32 v198, v196, v195
	v_med3_i32 v196, v196, v197, v195
	v_med3_i32 v194, v197, v194, v195
	v_and_or_b32 v195, v105, s26, 25
	v_max_i32_e32 v197, v198, v195
	v_med3_i32 v198, v198, v196, v195
	v_med3_i32 v194, v196, v194, v195
	v_and_or_b32 v195, v106, s26, 26
	v_max_i32_e32 v196, v197, v195
	v_med3_i32 v197, v197, v198, v195
	v_med3_i32 v194, v198, v194, v195
	v_and_or_b32 v195, v107, s26, 27
	v_max_i32_e32 v198, v196, v195
	v_med3_i32 v196, v196, v197, v195
	v_med3_i32 v194, v197, v194, v195
	v_and_or_b32 v195, v96, s26, 28
	v_max_i32_e32 v197, v198, v195
	v_med3_i32 v198, v198, v196, v195
	v_med3_i32 v194, v196, v194, v195
	v_and_or_b32 v195, v97, s26, 29
	v_ashrrev_i32_e32 v189, 6, v188
	v_max_i32_e32 v196, v197, v195
	v_med3_i32 v197, v197, v198, v195
	v_med3_i32 v194, v198, v194, v195
	v_and_or_b32 v195, v98, s26, 30
	v_and_b32_e32 v192, 63, v188
	v_lshl_add_u32 v191, v189, 12, s25
	v_max_i32_e32 v198, v196, v195
	v_med3_i32 v196, v196, v197, v195
	v_med3_i32 v194, v197, v194, v195
	v_and_or_b32 v195, v99, s26, 31
	v_lshl_add_u32 v192, v192, 4, v191
	v_med3_i32 v194, v196, v194, v195
	ds_write_b128 v192, v[212:215]
	v_max_i32_e32 v197, v198, v195
	v_med3_i32 v198, v198, v196, v195
	v_or_b32_e32 v214, v194, v193
	v_and_b32_e32 v194, 0xffffff80, v112
	v_and_or_b32 v195, v113, s26, 1
	v_or_b32_e32 v212, v197, v193
	v_or_b32_e32 v213, v198, v193
	v_max_i32_e32 v196, v194, v195
	v_min_i32_e32 v197, v194, v195
	v_and_or_b32 v198, v114, s26, 2
	v_max_i32_e32 v196, v196, v198
	v_med3_i32 v194, v194, v195, v198
	v_min_i32_e32 v195, v197, v198
	v_and_or_b32 v197, v115, s26, 3
	v_max_i32_e32 v198, v196, v197
	v_med3_i32 v196, v196, v194, v197
	v_min_i32_e32 v194, v194, v197
	v_max_i32_e32 v194, v195, v194
	v_and_or_b32 v195, v100, s26, 4
	v_max_i32_e32 v197, v198, v195
	v_med3_i32 v198, v198, v196, v195
	v_med3_i32 v194, v196, v194, v195
	v_and_or_b32 v195, v101, s26, 5
	v_max_i32_e32 v196, v197, v195
	v_med3_i32 v197, v197, v198, v195
	v_med3_i32 v194, v198, v194, v195
	v_and_or_b32 v195, v102, s26, 6
	v_max_i32_e32 v198, v196, v195
	v_med3_i32 v196, v196, v197, v195
	v_med3_i32 v194, v197, v194, v195
	v_and_or_b32 v195, v103, s26, 7
	v_max_i32_e32 v197, v198, v195
	v_med3_i32 v198, v198, v196, v195
	v_med3_i32 v194, v196, v194, v195
	v_and_or_b32 v195, v92, s26, 8
	v_max_i32_e32 v196, v197, v195
	v_med3_i32 v197, v197, v198, v195
	v_med3_i32 v194, v198, v194, v195
	v_and_or_b32 v195, v93, s26, 9
	v_max_i32_e32 v198, v196, v195
	v_med3_i32 v196, v196, v197, v195
	v_med3_i32 v194, v197, v194, v195
	v_and_or_b32 v195, v94, s26, 10
	v_max_i32_e32 v197, v198, v195
	v_med3_i32 v198, v198, v196, v195
	v_med3_i32 v194, v196, v194, v195
	v_and_or_b32 v195, v95, s26, 11
	v_max_i32_e32 v196, v197, v195
	v_med3_i32 v197, v197, v198, v195
	v_med3_i32 v194, v198, v194, v195
	v_and_or_b32 v195, v88, s26, 12
	v_max_i32_e32 v198, v196, v195
	v_med3_i32 v196, v196, v197, v195
	v_med3_i32 v194, v197, v194, v195
	v_and_or_b32 v195, v89, s26, 13
	v_max_i32_e32 v197, v198, v195
	v_med3_i32 v198, v198, v196, v195
	v_med3_i32 v194, v196, v194, v195
	v_and_or_b32 v195, v90, s26, 14
	v_max_i32_e32 v196, v197, v195
	v_med3_i32 v197, v197, v198, v195
	v_med3_i32 v194, v198, v194, v195
	v_and_or_b32 v195, v91, s26, 15
	v_max_i32_e32 v198, v196, v195
	v_med3_i32 v196, v196, v197, v195
	v_med3_i32 v194, v197, v194, v195
	v_and_or_b32 v195, v80, s26, 16
	v_max_i32_e32 v197, v198, v195
	v_med3_i32 v198, v198, v196, v195
	v_med3_i32 v194, v196, v194, v195
	v_and_or_b32 v195, v81, s26, 17
	v_max_i32_e32 v196, v197, v195
	v_med3_i32 v197, v197, v198, v195
	v_med3_i32 v194, v198, v194, v195
	v_and_or_b32 v195, v82, s26, 18
	v_max_i32_e32 v198, v196, v195
	v_med3_i32 v196, v196, v197, v195
	v_med3_i32 v194, v197, v194, v195
	v_and_or_b32 v195, v83, s26, 19
	v_max_i32_e32 v197, v198, v195
	v_med3_i32 v198, v198, v196, v195
	v_med3_i32 v194, v196, v194, v195
	v_and_or_b32 v195, v72, s26, 20
	v_max_i32_e32 v196, v197, v195
	v_med3_i32 v197, v197, v198, v195
	v_med3_i32 v194, v198, v194, v195
	v_and_or_b32 v195, v73, s26, 21
	v_max_i32_e32 v198, v196, v195
	v_med3_i32 v196, v196, v197, v195
	v_med3_i32 v194, v197, v194, v195
	v_and_or_b32 v195, v74, s26, 22
	v_max_i32_e32 v197, v198, v195
	v_med3_i32 v198, v198, v196, v195
	v_med3_i32 v194, v196, v194, v195
	v_and_or_b32 v195, v75, s26, 23
	v_max_i32_e32 v196, v197, v195
	v_med3_i32 v197, v197, v198, v195
	v_med3_i32 v194, v198, v194, v195
	v_and_or_b32 v195, v64, s26, 24
	v_max_i32_e32 v198, v196, v195
	v_med3_i32 v196, v196, v197, v195
	v_med3_i32 v194, v197, v194, v195
	v_and_or_b32 v195, v65, s26, 25
	v_max_i32_e32 v197, v198, v195
	v_med3_i32 v198, v198, v196, v195
	v_med3_i32 v194, v196, v194, v195
	v_and_or_b32 v195, v66, s26, 26
	v_max_i32_e32 v196, v197, v195
	v_med3_i32 v197, v197, v198, v195
	v_med3_i32 v194, v198, v194, v195
	v_and_or_b32 v195, v67, s26, 27
	v_max_i32_e32 v198, v196, v195
	v_med3_i32 v196, v196, v197, v195
	v_med3_i32 v194, v197, v194, v195
	v_and_or_b32 v195, v56, s26, 28
	v_max_i32_e32 v197, v198, v195
	v_med3_i32 v198, v198, v196, v195
	v_med3_i32 v194, v196, v194, v195
	v_and_or_b32 v195, v57, s26, 29
	v_max_i32_e32 v196, v197, v195
	v_med3_i32 v197, v197, v198, v195
	v_med3_i32 v194, v198, v194, v195
	v_and_or_b32 v195, v58, s26, 30
	v_max_i32_e32 v198, v196, v195
	v_med3_i32 v196, v196, v197, v195
	v_med3_i32 v194, v197, v194, v195
	v_and_or_b32 v195, v59, s26, 31
	v_med3_i32 v194, v196, v194, v195
	ds_write_b128 v192, v[212:215] offset:1024
	s_waitcnt vmcnt(0)
	s_barrier
	s_and_b64 vcc, exec, s[10:11]
	s_cbranch_vccnz .Lmid_skip
	s_add_u32 s68, s68, 0x6000
	s_addc_u32 s69, s69, 0
	s_add_u32 s70, s70, 0x6000
	s_addc_u32 s71, s71, 0
	s_mov_b32 m0, s77
	s_nop 0
	global_load_lds_dwordx4 v228, s[68:69] offset:-3072
	global_load_lds_dwordx4 v228, s[68:69] offset:-2048
	global_load_lds_dwordx4 v228, s[68:69] offset:-1024
	global_load_lds_dwordx4 v228, s[68:69]
	global_load_lds_dwordx4 v228, s[68:69] offset:1024
	global_load_lds_dwordx4 v228, s[68:69] offset:2048
	ds_read_b128 v[2:5], v170 offset:12288
	ds_read_b64 v[6:7], v173 offset:12352
	ds_read_b128 v[8:11], v170 offset:13824
	ds_read_b64 v[12:13], v173 offset:13888
	ds_read_b128 v[14:17], v170 offset:15360
	ds_read_b64 v[18:19], v173 offset:15424
	ds_read_b128 v[26:29], v170 offset:16896
	ds_read_b64 v[30:31], v173 offset:16960
	ds_read_b128 v[20:23], v1
	ds_read_b64 v[24:25], v172 offset:64
	ds_read_b128 v[32:35], v1 offset:1536
	ds_read_b64 v[36:37], v172 offset:1600

.LBB1_2:
	s_mul_i32 s41, s34, 0x30000
	s_mul_hi_i32 s40, s34, 0x30000
	s_add_u32 s11, s6, s41
	s_addc_u32 s35, s7, s40
	s_mov_b32 s10, s2
	s_add_u32 s2, s11, 0x6000
	s_addc_u32 s3, s35, 0
	s_mul_i32 s43, s13, 0x30000
	s_mul_hi_i32 s42, s13, 0x30000
	s_add_u32 s44, s4, s43
	s_addc_u32 s45, s5, s42
	s_add_u32 s38, s11, 0x8000
	s_addc_u32 s39, s35, 0
	s_add_u32 s46, s44, 0x5000
	s_addc_u32 s47, s45, 0
	s_and_b64 s[36:37], s[0:1], exec
	s_cselect_b32 s37, s39, s47
	s_cselect_b32 s36, s38, s46
	s_add_u32 s38, s44, 0x7000
	s_addc_u32 s39, s45, 0
	s_add_u32 s2, s11, 0x9000
	s_addc_u32 s3, s35, 0
	s_add_u32 s11, s11, 0xb000
	s_addc_u32 s35, s35, 0
	s_add_u32 s38, s44, 0x8000
	s_addc_u32 s39, s45, 0
	s_and_b64 s[36:37], s[0:1], exec
	s_cselect_b32 s37, s35, s39
	s_cselect_b32 s36, s11, s38
	s_add_u32 s38, s44, 0xa000
	s_addc_u32 s39, s45, 0
	s_add_u32 s11, s21, s43
	s_addc_u32 s35, s22, s42
	s_add_u32 s2, s23, s41
	s_addc_u32 s3, s24, s40
	s_cmp_eq_u32 s74, 1
	s_cselect_b32 s72, s11, s2
	s_cselect_b32 s73, s35, s3
	s_add_u32 s72, s72, s75
	s_addc_u32 s73, s73, 0
	s_mov_b32 s36, -2
	s_waitcnt lgkmcnt(0)
.Lgemm_peel:
	ds_read_b128 v[188:191], v1 offset:24576
	ds_read_b64 v[192:193], v172 offset:24640
	ds_read_b128 v[194:197], v1 offset:26112
	ds_read_b64 v[198:199], v172 offset:26176
	ds_read_b128 v[200:203], v170 offset:36864
	ds_read_b64 v[204:205], v173 offset:36928
	ds_read_b128 v[206:209], v170 offset:38400
	ds_read_b64 v[210:211], v173 offset:38464
	ds_read_b128 v[212:215], v170 offset:39936
	ds_read_b64 v[216:217], v173 offset:40000
	ds_read_b128 v[218:221], v170 offset:41472
	ds_read_b64 v[222:223], v173 offset:41536
	v_mfma_scale_f32_16x16x128_f8f6f4 v[164:167], v[2:7], v[20:25], 0, v187, v187 op_sel_hi:[0,0,0] cbsz:2 blgp:2
	v_mfma_scale_f32_16x16x128_f8f6f4 v[160:163], v[8:13], v[20:25], 0, v187, v187 op_sel_hi:[0,0,0] cbsz:2 blgp:2
	v_mfma_scale_f32_16x16x128_f8f6f4 v[156:159], v[14:19], v[20:25], 0, v187, v187 op_sel_hi:[0,0,0] cbsz:2 blgp:2
	v_mfma_scale_f32_16x16x128_f8f6f4 v[152:155], v[26:31], v[20:25], 0, v187, v187 op_sel_hi:[0,0,0] cbsz:2 blgp:2
	v_mfma_scale_f32_16x16x128_f8f6f4 v[148:151], v[2:7], v[32:37], 0, v187, v187 op_sel_hi:[0,0,0] cbsz:2 blgp:2
	v_mfma_scale_f32_16x16x128_f8f6f4 v[140:143], v[8:13], v[32:37], 0, v187, v187 op_sel_hi:[0,0,0] cbsz:2 blgp:2
	v_mfma_scale_f32_16x16x128_f8f6f4 v[132:135], v[14:19], v[32:37], 0, v187, v187 op_sel_hi:[0,0,0] cbsz:2 blgp:2
	v_mfma_scale_f32_16x16x128_f8f6f4 v[124:127], v[26:31], v[32:37], 0, v187, v187 op_sel_hi:[0,0,0] cbsz:2 blgp:2
	s_cmp_eq_u32 s66, 0
	s_cbranch_scc0 .Lpst0_other
	s_add_u32 s38, s72, 0xffffa000
	s_addc_u32 s39, s73, -1
	s_waitcnt vmcnt(0)
	s_barrier
	s_mov_b32 m0, s76
	s_nop 0
	global_load_lds_dwordx4 v228, s[38:39] offset:-3072
	global_load_lds_dwordx4 v228, s[38:39] offset:-2048
	global_load_lds_dwordx4 v228, s[38:39] offset:-1024
	global_load_lds_dwordx4 v228, s[38:39]
	global_load_lds_dwordx4 v228, s[38:39] offset:1024
	global_load_lds_dwordx4 v228, s[38:39] offset:2048
	s_branch .Lpst0_join

.Lpst0_join:
	s_waitcnt lgkmcnt(0)
	v_mfma_scale_f32_16x16x128_f8f6f4 v[112:115], v[2:7], v[188:193], 0, v187, v187 op_sel_hi:[0,0,0] cbsz:2 blgp:2
	v_mfma_scale_f32_16x16x128_f8f6f4 v[100:103], v[8:13], v[188:193], 0, v187, v187 op_sel_hi:[0,0,0] cbsz:2 blgp:2
	v_mfma_scale_f32_16x16x128_f8f6f4 v[92:95], v[14:19], v[188:193], 0, v187, v187 op_sel_hi:[0,0,0] cbsz:2 blgp:2
	v_mfma_scale_f32_16x16x128_f8f6f4 v[88:91], v[26:31], v[188:193], 0, v187, v187 op_sel_hi:[0,0,0] cbsz:2 blgp:2
	v_mfma_scale_f32_16x16x128_f8f6f4 v[84:87], v[2:7], v[194:199], 0, v187, v187 op_sel_hi:[0,0,0] cbsz:2 blgp:2
	v_mfma_scale_f32_16x16x128_f8f6f4 v[76:79], v[8:13], v[194:199], 0, v187, v187 op_sel_hi:[0,0,0] cbsz:2 blgp:2
	v_mfma_scale_f32_16x16x128_f8f6f4 v[68:71], v[14:19], v[194:199], 0, v187, v187 op_sel_hi:[0,0,0] cbsz:2 blgp:2
	v_mfma_scale_f32_16x16x128_f8f6f4 v[60:63], v[26:31], v[194:199], 0, v187, v187 op_sel_hi:[0,0,0] cbsz:2 blgp:2
	ds_read_b128 v[2:5], v170 offset:61440
	ds_read_b64 v[6:7], v173 offset:61504
	ds_read_b128 v[8:11], v170 offset:62976
	ds_read_b64 v[12:13], v173 offset:63040
	ds_read_b128 v[14:17], v170 offset:64512
	ds_read_b64 v[18:19], v173 offset:64576
	ds_read_b128 v[26:29], v171 offset:53760
	ds_read_b64 v[30:31], v174 offset:53760
	v_mfma_scale_f32_16x16x128_f8f6f4 v[144:147], v[200:205], v[20:25], 0, v187, v187 op_sel_hi:[0,0,0] cbsz:2 blgp:2
	v_mfma_scale_f32_16x16x128_f8f6f4 v[136:139], v[206:211], v[20:25], 0, v187, v187 op_sel_hi:[0,0,0] cbsz:2 blgp:2
	v_mfma_scale_f32_16x16x128_f8f6f4 v[128:131], v[212:217], v[20:25], 0, v187, v187 op_sel_hi:[0,0,0] cbsz:2 blgp:2
	v_mfma_scale_f32_16x16x128_f8f6f4 v[120:123], v[218:223], v[20:25], 0, v187, v187 op_sel_hi:[0,0,0] cbsz:2 blgp:2
	v_mfma_scale_f32_16x16x128_f8f6f4 v[116:119], v[200:205], v[32:37], 0, v187, v187 op_sel_hi:[0,0,0] cbsz:2 blgp:2
	v_mfma_scale_f32_16x16x128_f8f6f4 v[108:111], v[206:211], v[32:37], 0, v187, v187 op_sel_hi:[0,0,0] cbsz:2 blgp:2
	v_mfma_scale_f32_16x16x128_f8f6f4 v[104:107], v[212:217], v[32:37], 0, v187, v187 op_sel_hi:[0,0,0] cbsz:2 blgp:2
	v_mfma_scale_f32_16x16x128_f8f6f4 v[96:99], v[218:223], v[32:37], 0, v187, v187 op_sel_hi:[0,0,0] cbsz:2 blgp:2
	ds_read_b128 v[20:23], v1 offset:49152
	ds_read_b64 v[24:25], v172 offset:49216
	ds_read_b128 v[32:35], v1 offset:50688
	ds_read_b64 v[36:37], v172 offset:50752
	s_cmp_eq_u32 s66, 1
	s_cbranch_scc0 .Lpst1_other
	s_add_u32 s38, s72, 0xffffd000
	s_addc_u32 s39, s73, -1
	s_waitcnt vmcnt(0)
	s_barrier
	s_mov_b32 m0, s76
	s_nop 0
	global_load_lds_dwordx4 v228, s[38:39] offset:-3072
	global_load_lds_dwordx4 v228, s[38:39] offset:-2048
	global_load_lds_dwordx4 v228, s[38:39] offset:-1024
	global_load_lds_dwordx4 v228, s[38:39]
	global_load_lds_dwordx4 v228, s[38:39] offset:1024
	global_load_lds_dwordx4 v228, s[38:39] offset:2048
	s_branch .Lpst1_join

.Lpst1_join:
	v_mfma_scale_f32_16x16x128_f8f6f4 v[80:83], v[200:205], v[188:193], 0, v187, v187 op_sel_hi:[0,0,0] cbsz:2 blgp:2
	v_mfma_scale_f32_16x16x128_f8f6f4 v[72:75], v[206:211], v[188:193], 0, v187, v187 op_sel_hi:[0,0,0] cbsz:2 blgp:2
	v_mfma_scale_f32_16x16x128_f8f6f4 v[64:67], v[212:217], v[188:193], 0, v187, v187 op_sel_hi:[0,0,0] cbsz:2 blgp:2
	v_mfma_scale_f32_16x16x128_f8f6f4 v[56:59], v[218:223], v[188:193], 0, v187, v187 op_sel_hi:[0,0,0] cbsz:2 blgp:2
	v_mfma_scale_f32_16x16x128_f8f6f4 v[52:55], v[200:205], v[194:199], 0, v187, v187 op_sel_hi:[0,0,0] cbsz:2 blgp:2
	v_mfma_scale_f32_16x16x128_f8f6f4 v[224:227], v[206:211], v[194:199], 0, v187, v187 op_sel_hi:[0,0,0] cbsz:2 blgp:2
	v_mfma_scale_f32_16x16x128_f8f6f4 v[212:215], v[212:217], v[194:199], 0, v187, v187 op_sel_hi:[0,0,0] cbsz:2 blgp:2
	v_mfma_scale_f32_16x16x128_f8f6f4 v[216:219], v[218:223], v[194:199], 0, v187, v187 op_sel_hi:[0,0,0] cbsz:2 blgp:2
	s_waitcnt lgkmcnt(0)
	s_nop 0
	ds_read_b128 v[40:43], v175
	ds_read_b64 v[44:45], v176
	ds_read_b128 v[188:191], v179
	ds_read_b64 v[192:193], v180
	ds_read_b128 v[46:49], v177
	ds_read_b64 v[50:51], v178
	ds_read_b128 v[194:197], v181
	ds_read_b64 v[198:199], v182
	ds_read_b128 v[200:203], v183
	ds_read_b64 v[204:205], v184
	ds_read_b128 v[206:209], v185
	ds_read_b64 v[210:211], v186
	v_mfma_scale_f32_16x16x128_f8f6f4 v[164:167], v[2:7], v[20:25], v[164:167], v187, v187 op_sel_hi:[0,0,0] cbsz:2 blgp:2
	v_mfma_scale_f32_16x16x128_f8f6f4 v[160:163], v[8:13], v[20:25], v[160:163], v187, v187 op_sel_hi:[0,0,0] cbsz:2 blgp:2
	v_mfma_scale_f32_16x16x128_f8f6f4 v[156:159], v[14:19], v[20:25], v[156:159], v187, v187 op_sel_hi:[0,0,0] cbsz:2 blgp:2
	v_mfma_scale_f32_16x16x128_f8f6f4 v[152:155], v[26:31], v[20:25], v[152:155], v187, v187 op_sel_hi:[0,0,0] cbsz:2 blgp:2
	v_mfma_scale_f32_16x16x128_f8f6f4 v[148:151], v[2:7], v[32:37], v[148:151], v187, v187 op_sel_hi:[0,0,0] cbsz:2 blgp:2
	v_mfma_scale_f32_16x16x128_f8f6f4 v[140:143], v[8:13], v[32:37], v[140:143], v187, v187 op_sel_hi:[0,0,0] cbsz:2 blgp:2
	v_mfma_scale_f32_16x16x128_f8f6f4 v[132:135], v[14:19], v[32:37], v[132:135], v187, v187 op_sel_hi:[0,0,0] cbsz:2 blgp:2
	v_mfma_scale_f32_16x16x128_f8f6f4 v[124:127], v[26:31], v[32:37], v[124:127], v187, v187 op_sel_hi:[0,0,0] cbsz:2 blgp:2
	s_cmp_eq_u32 s66, 0
	s_cbranch_scc0 .Lpst2_other
	s_mov_b64 s[38:39], s[72:73]
	s_waitcnt vmcnt(0)
	s_barrier
	s_mov_b32 m0, s77
	s_nop 0
	global_load_lds_dwordx4 v228, s[38:39] offset:-3072
	global_load_lds_dwordx4 v228, s[38:39] offset:-2048
	global_load_lds_dwordx4 v228, s[38:39] offset:-1024
	global_load_lds_dwordx4 v228, s[38:39]
	global_load_lds_dwordx4 v228, s[38:39] offset:1024
	global_load_lds_dwordx4 v228, s[38:39] offset:2048
	s_branch .Lpst2_join

.Lpst2_join:
	s_waitcnt lgkmcnt(0)
	v_mfma_scale_f32_16x16x128_f8f6f4 v[112:115], v[2:7], v[40:45], v[112:115], v187, v187 op_sel_hi:[0,0,0] cbsz:2 blgp:2
	v_mfma_scale_f32_16x16x128_f8f6f4 v[100:103], v[8:13], v[40:45], v[100:103], v187, v187 op_sel_hi:[0,0,0] cbsz:2 blgp:2
	v_mfma_scale_f32_16x16x128_f8f6f4 v[92:95], v[14:19], v[40:45], v[92:95], v187, v187 op_sel_hi:[0,0,0] cbsz:2 blgp:2
	v_mfma_scale_f32_16x16x128_f8f6f4 v[88:91], v[26:31], v[40:45], v[88:91], v187, v187 op_sel_hi:[0,0,0] cbsz:2 blgp:2
	v_mfma_scale_f32_16x16x128_f8f6f4 v[84:87], v[2:7], v[188:193], v[84:87], v187, v187 op_sel_hi:[0,0,0] cbsz:2 blgp:2
	v_mfma_scale_f32_16x16x128_f8f6f4 v[76:79], v[8:13], v[188:193], v[76:79], v187, v187 op_sel_hi:[0,0,0] cbsz:2 blgp:2
	v_mfma_scale_f32_16x16x128_f8f6f4 v[68:71], v[14:19], v[188:193], v[68:71], v187, v187 op_sel_hi:[0,0,0] cbsz:2 blgp:2
	v_mfma_scale_f32_16x16x128_f8f6f4 v[60:63], v[26:31], v[188:193], v[60:63], v187, v187 op_sel_hi:[0,0,0] cbsz:2 blgp:2
	ds_read_b128 v[2:5], v170 offset:12288
	ds_read_b64 v[6:7], v173 offset:12352
	ds_read_b128 v[8:11], v170 offset:13824
	ds_read_b64 v[12:13], v173 offset:13888
	ds_read_b128 v[14:17], v170 offset:15360
	ds_read_b64 v[18:19], v173 offset:15424
	ds_read_b128 v[26:29], v170 offset:16896
	ds_read_b64 v[30:31], v173 offset:16960
	v_mfma_scale_f32_16x16x128_f8f6f4 v[144:147], v[46:51], v[20:25], v[144:147], v187, v187 op_sel_hi:[0,0,0] cbsz:2 blgp:2
	v_mfma_scale_f32_16x16x128_f8f6f4 v[136:139], v[194:199], v[20:25], v[136:139], v187, v187 op_sel_hi:[0,0,0] cbsz:2 blgp:2
	v_mfma_scale_f32_16x16x128_f8f6f4 v[128:131], v[200:205], v[20:25], v[128:131], v187, v187 op_sel_hi:[0,0,0] cbsz:2 blgp:2
	v_mfma_scale_f32_16x16x128_f8f6f4 v[120:123], v[206:211], v[20:25], v[120:123], v187, v187 op_sel_hi:[0,0,0] cbsz:2 blgp:2
	v_mfma_scale_f32_16x16x128_f8f6f4 v[116:119], v[46:51], v[32:37], v[116:119], v187, v187 op_sel_hi:[0,0,0] cbsz:2 blgp:2
	v_mfma_scale_f32_16x16x128_f8f6f4 v[108:111], v[194:199], v[32:37], v[108:111], v187, v187 op_sel_hi:[0,0,0] cbsz:2 blgp:2
	v_mfma_scale_f32_16x16x128_f8f6f4 v[104:107], v[200:205], v[32:37], v[104:107], v187, v187 op_sel_hi:[0,0,0] cbsz:2 blgp:2
	v_mfma_scale_f32_16x16x128_f8f6f4 v[96:99], v[206:211], v[32:37], v[96:99], v187, v187 op_sel_hi:[0,0,0] cbsz:2 blgp:2
	ds_read_b128 v[20:23], v1
	ds_read_b64 v[24:25], v172 offset:64
	ds_read_b128 v[32:35], v1 offset:1536
	ds_read_b64 v[36:37], v172 offset:1600
	s_cmp_eq_u32 s66, 1
	s_cbranch_scc0 .Lpst3_other
	s_add_u32 s38, s72, 0x3000
	s_addc_u32 s39, s73, 0
	s_waitcnt vmcnt(0)
	s_barrier
	s_mov_b32 m0, s77
	s_nop 0
	global_load_lds_dwordx4 v228, s[38:39] offset:-3072
	global_load_lds_dwordx4 v228, s[38:39] offset:-2048
	global_load_lds_dwordx4 v228, s[38:39] offset:-1024
	global_load_lds_dwordx4 v228, s[38:39]
	global_load_lds_dwordx4 v228, s[38:39] offset:1024
	global_load_lds_dwordx4 v228, s[38:39] offset:2048
	s_branch .Lpst3_join

.Lpst3_join:
	v_mfma_scale_f32_16x16x128_f8f6f4 v[80:83], v[46:51], v[40:45], v[80:83], v187, v187 op_sel_hi:[0,0,0] cbsz:2 blgp:2
	v_mfma_scale_f32_16x16x128_f8f6f4 v[72:75], v[194:199], v[40:45], v[72:75], v187, v187 op_sel_hi:[0,0,0] cbsz:2 blgp:2
	v_mfma_scale_f32_16x16x128_f8f6f4 v[64:67], v[200:205], v[40:45], v[64:67], v187, v187 op_sel_hi:[0,0,0] cbsz:2 blgp:2
	v_mfma_scale_f32_16x16x128_f8f6f4 v[56:59], v[206:211], v[40:45], v[56:59], v187, v187 op_sel_hi:[0,0,0] cbsz:2 blgp:2
	v_mfma_scale_f32_16x16x128_f8f6f4 v[52:55], v[46:51], v[188:193], v[52:55], v187, v187 op_sel_hi:[0,0,0] cbsz:2 blgp:2
	v_mfma_scale_f32_16x16x128_f8f6f4 v[48:51], v[194:199], v[188:193], v[224:227], v187, v187 op_sel_hi:[0,0,0] cbsz:2 blgp:2
	v_mfma_scale_f32_16x16x128_f8f6f4 v[44:47], v[200:205], v[188:193], v[212:215], v187, v187 op_sel_hi:[0,0,0] cbsz:2 blgp:2
	v_mfma_scale_f32_16x16x128_f8f6f4 v[40:43], v[206:211], v[188:193], v[216:219], v187, v187 op_sel_hi:[0,0,0] cbsz:2 blgp:2
	s_add_i32 s36, s36, 2
	s_add_u32 s11, s11, 0xc000
	s_addc_u32 s35, s35, 0
	s_add_u32 s2, s2, 0xc000
	s_addc_u32 s3, s3, 0
	s_add_u32 s72, s72, 0xc000
	s_addc_u32 s73, s73, 0
	s_cmp_lt_u32 s36, 4
	s_waitcnt lgkmcnt(0)
.LBB1_3:
	ds_read_b128 v[188:191], v1 offset:24576
	ds_read_b64 v[192:193], v172 offset:24640
	ds_read_b128 v[194:197], v1 offset:26112
	ds_read_b64 v[198:199], v172 offset:26176
	ds_read_b128 v[200:203], v170 offset:36864
	ds_read_b64 v[204:205], v173 offset:36928
	ds_read_b128 v[206:209], v170 offset:38400
	ds_read_b64 v[210:211], v173 offset:38464
	ds_read_b128 v[212:215], v170 offset:39936
	ds_read_b64 v[216:217], v173 offset:40000
	ds_read_b128 v[218:221], v170 offset:41472
	ds_read_b64 v[222:223], v173 offset:41536
	v_mfma_scale_f32_16x16x128_f8f6f4 v[164:167], v[2:7], v[20:25], v[164:167], v187, v187 op_sel_hi:[0,0,0] cbsz:2 blgp:2
	v_mfma_scale_f32_16x16x128_f8f6f4 v[160:163], v[8:13], v[20:25], v[160:163], v187, v187 op_sel_hi:[0,0,0] cbsz:2 blgp:2
	v_mfma_scale_f32_16x16x128_f8f6f4 v[156:159], v[14:19], v[20:25], v[156:159], v187, v187 op_sel_hi:[0,0,0] cbsz:2 blgp:2
	v_mfma_scale_f32_16x16x128_f8f6f4 v[152:155], v[26:31], v[20:25], v[152:155], v187, v187 op_sel_hi:[0,0,0] cbsz:2 blgp:2
	v_mfma_scale_f32_16x16x128_f8f6f4 v[148:151], v[2:7], v[32:37], v[148:151], v187, v187 op_sel_hi:[0,0,0] cbsz:2 blgp:2
	v_mfma_scale_f32_16x16x128_f8f6f4 v[140:143], v[8:13], v[32:37], v[140:143], v187, v187 op_sel_hi:[0,0,0] cbsz:2 blgp:2
	v_mfma_scale_f32_16x16x128_f8f6f4 v[132:135], v[14:19], v[32:37], v[132:135], v187, v187 op_sel_hi:[0,0,0] cbsz:2 blgp:2
	v_mfma_scale_f32_16x16x128_f8f6f4 v[124:127], v[26:31], v[32:37], v[124:127], v187, v187 op_sel_hi:[0,0,0] cbsz:2 blgp:2
	s_cmp_eq_u32 s66, 0
	s_cbranch_scc0 .Lst0_other
	s_add_u32 s38, s72, 0xffffa000
	s_addc_u32 s39, s73, -1
	s_waitcnt vmcnt(0)
	s_barrier
	s_mov_b32 m0, s76
	s_nop 0
	global_load_lds_dwordx4 v228, s[38:39] offset:-3072
	global_load_lds_dwordx4 v228, s[38:39] offset:-2048
	global_load_lds_dwordx4 v228, s[38:39] offset:-1024
	global_load_lds_dwordx4 v228, s[38:39]
	global_load_lds_dwordx4 v228, s[38:39] offset:1024
	global_load_lds_dwordx4 v228, s[38:39] offset:2048
	s_branch .Lst0_join

.Lst0_join:
	s_waitcnt lgkmcnt(0)
	v_mfma_scale_f32_16x16x128_f8f6f4 v[112:115], v[2:7], v[188:193], v[112:115], v187, v187 op_sel_hi:[0,0,0] cbsz:2 blgp:2
	v_mfma_scale_f32_16x16x128_f8f6f4 v[100:103], v[8:13], v[188:193], v[100:103], v187, v187 op_sel_hi:[0,0,0] cbsz:2 blgp:2
	v_mfma_scale_f32_16x16x128_f8f6f4 v[92:95], v[14:19], v[188:193], v[92:95], v187, v187 op_sel_hi:[0,0,0] cbsz:2 blgp:2
	v_mfma_scale_f32_16x16x128_f8f6f4 v[88:91], v[26:31], v[188:193], v[88:91], v187, v187 op_sel_hi:[0,0,0] cbsz:2 blgp:2
	v_mfma_scale_f32_16x16x128_f8f6f4 v[84:87], v[2:7], v[194:199], v[84:87], v187, v187 op_sel_hi:[0,0,0] cbsz:2 blgp:2
	v_mfma_scale_f32_16x16x128_f8f6f4 v[76:79], v[8:13], v[194:199], v[76:79], v187, v187 op_sel_hi:[0,0,0] cbsz:2 blgp:2
	v_mfma_scale_f32_16x16x128_f8f6f4 v[68:71], v[14:19], v[194:199], v[68:71], v187, v187 op_sel_hi:[0,0,0] cbsz:2 blgp:2
	v_mfma_scale_f32_16x16x128_f8f6f4 v[60:63], v[26:31], v[194:199], v[60:63], v187, v187 op_sel_hi:[0,0,0] cbsz:2 blgp:2
	ds_read_b128 v[2:5], v170 offset:61440
	ds_read_b64 v[6:7], v173 offset:61504
	ds_read_b128 v[8:11], v170 offset:62976
	ds_read_b64 v[12:13], v173 offset:63040
	ds_read_b128 v[14:17], v170 offset:64512
	ds_read_b64 v[18:19], v173 offset:64576
	ds_read_b128 v[26:29], v171 offset:53760
	ds_read_b64 v[30:31], v174 offset:53760
	v_mfma_scale_f32_16x16x128_f8f6f4 v[144:147], v[200:205], v[20:25], v[144:147], v187, v187 op_sel_hi:[0,0,0] cbsz:2 blgp:2
	v_mfma_scale_f32_16x16x128_f8f6f4 v[136:139], v[206:211], v[20:25], v[136:139], v187, v187 op_sel_hi:[0,0,0] cbsz:2 blgp:2
	v_mfma_scale_f32_16x16x128_f8f6f4 v[128:131], v[212:217], v[20:25], v[128:131], v187, v187 op_sel_hi:[0,0,0] cbsz:2 blgp:2
	v_mfma_scale_f32_16x16x128_f8f6f4 v[120:123], v[218:223], v[20:25], v[120:123], v187, v187 op_sel_hi:[0,0,0] cbsz:2 blgp:2
	v_mfma_scale_f32_16x16x128_f8f6f4 v[116:119], v[200:205], v[32:37], v[116:119], v187, v187 op_sel_hi:[0,0,0] cbsz:2 blgp:2
	v_mfma_scale_f32_16x16x128_f8f6f4 v[108:111], v[206:211], v[32:37], v[108:111], v187, v187 op_sel_hi:[0,0,0] cbsz:2 blgp:2
	v_mfma_scale_f32_16x16x128_f8f6f4 v[104:107], v[212:217], v[32:37], v[104:107], v187, v187 op_sel_hi:[0,0,0] cbsz:2 blgp:2
	v_mfma_scale_f32_16x16x128_f8f6f4 v[96:99], v[218:223], v[32:37], v[96:99], v187, v187 op_sel_hi:[0,0,0] cbsz:2 blgp:2
	ds_read_b128 v[20:23], v1 offset:49152
	ds_read_b64 v[24:25], v172 offset:49216
	ds_read_b128 v[32:35], v1 offset:50688
	ds_read_b64 v[36:37], v172 offset:50752
	s_cmp_eq_u32 s66, 1
	s_cbranch_scc0 .Lst1_other
	s_add_u32 s38, s72, 0xffffd000
	s_addc_u32 s39, s73, -1
	s_waitcnt vmcnt(0)
	s_barrier
	s_mov_b32 m0, s76
	s_nop 0
	global_load_lds_dwordx4 v228, s[38:39] offset:-3072
	global_load_lds_dwordx4 v228, s[38:39] offset:-2048
	global_load_lds_dwordx4 v228, s[38:39] offset:-1024
	global_load_lds_dwordx4 v228, s[38:39]
	global_load_lds_dwordx4 v228, s[38:39] offset:1024
	global_load_lds_dwordx4 v228, s[38:39] offset:2048
	s_branch .Lst1_join

.Lst1_join:
	v_mfma_scale_f32_16x16x128_f8f6f4 v[80:83], v[200:205], v[188:193], v[80:83], v187, v187 op_sel_hi:[0,0,0] cbsz:2 blgp:2
	v_mfma_scale_f32_16x16x128_f8f6f4 v[72:75], v[206:211], v[188:193], v[72:75], v187, v187 op_sel_hi:[0,0,0] cbsz:2 blgp:2
	v_mfma_scale_f32_16x16x128_f8f6f4 v[64:67], v[212:217], v[188:193], v[64:67], v187, v187 op_sel_hi:[0,0,0] cbsz:2 blgp:2
	v_mfma_scale_f32_16x16x128_f8f6f4 v[56:59], v[218:223], v[188:193], v[56:59], v187, v187 op_sel_hi:[0,0,0] cbsz:2 blgp:2
	v_mfma_scale_f32_16x16x128_f8f6f4 v[52:55], v[200:205], v[194:199], v[52:55], v187, v187 op_sel_hi:[0,0,0] cbsz:2 blgp:2
	v_mfma_scale_f32_16x16x128_f8f6f4 v[224:227], v[206:211], v[194:199], v[48:51], v187, v187 op_sel_hi:[0,0,0] cbsz:2 blgp:2
	v_mfma_scale_f32_16x16x128_f8f6f4 v[212:215], v[212:217], v[194:199], v[44:47], v187, v187 op_sel_hi:[0,0,0] cbsz:2 blgp:2
	v_mfma_scale_f32_16x16x128_f8f6f4 v[216:219], v[218:223], v[194:199], v[40:43], v187, v187 op_sel_hi:[0,0,0] cbsz:2 blgp:2
	s_waitcnt lgkmcnt(0)
	s_nop 0
	ds_read_b128 v[40:43], v175
	ds_read_b64 v[44:45], v176
	ds_read_b128 v[188:191], v179
	ds_read_b64 v[192:193], v180
	ds_read_b128 v[46:49], v177
	ds_read_b64 v[50:51], v178
	ds_read_b128 v[194:197], v181
	ds_read_b64 v[198:199], v182
	ds_read_b128 v[200:203], v183
	ds_read_b64 v[204:205], v184
	ds_read_b128 v[206:209], v185
	ds_read_b64 v[210:211], v186
	v_mfma_scale_f32_16x16x128_f8f6f4 v[164:167], v[2:7], v[20:25], v[164:167], v187, v187 op_sel_hi:[0,0,0] cbsz:2 blgp:2
	v_mfma_scale_f32_16x16x128_f8f6f4 v[160:163], v[8:13], v[20:25], v[160:163], v187, v187 op_sel_hi:[0,0,0] cbsz:2 blgp:2
	v_mfma_scale_f32_16x16x128_f8f6f4 v[156:159], v[14:19], v[20:25], v[156:159], v187, v187 op_sel_hi:[0,0,0] cbsz:2 blgp:2
	v_mfma_scale_f32_16x16x128_f8f6f4 v[152:155], v[26:31], v[20:25], v[152:155], v187, v187 op_sel_hi:[0,0,0] cbsz:2 blgp:2
	v_mfma_scale_f32_16x16x128_f8f6f4 v[148:151], v[2:7], v[32:37], v[148:151], v187, v187 op_sel_hi:[0,0,0] cbsz:2 blgp:2
	v_mfma_scale_f32_16x16x128_f8f6f4 v[140:143], v[8:13], v[32:37], v[140:143], v187, v187 op_sel_hi:[0,0,0] cbsz:2 blgp:2
	v_mfma_scale_f32_16x16x128_f8f6f4 v[132:135], v[14:19], v[32:37], v[132:135], v187, v187 op_sel_hi:[0,0,0] cbsz:2 blgp:2
	v_mfma_scale_f32_16x16x128_f8f6f4 v[124:127], v[26:31], v[32:37], v[124:127], v187, v187 op_sel_hi:[0,0,0] cbsz:2 blgp:2
	s_cmp_eq_u32 s66, 0
	s_cbranch_scc0 .Lst2_other
	s_mov_b64 s[38:39], s[72:73]
	s_waitcnt vmcnt(0)
	s_barrier
	s_mov_b32 m0, s77
	s_nop 0
	global_load_lds_dwordx4 v228, s[38:39] offset:-3072
	global_load_lds_dwordx4 v228, s[38:39] offset:-2048
	global_load_lds_dwordx4 v228, s[38:39] offset:-1024
	global_load_lds_dwordx4 v228, s[38:39]
	global_load_lds_dwordx4 v228, s[38:39] offset:1024
	global_load_lds_dwordx4 v228, s[38:39] offset:2048
	s_branch .Lst2_join

.Lst3_join:
	v_mfma_scale_f32_16x16x128_f8f6f4 v[80:83], v[46:51], v[40:45], v[80:83], v187, v187 op_sel_hi:[0,0,0] cbsz:2 blgp:2
	v_mfma_scale_f32_16x16x128_f8f6f4 v[72:75], v[194:199], v[40:45], v[72:75], v187, v187 op_sel_hi:[0,0,0] cbsz:2 blgp:2
	v_mfma_scale_f32_16x16x128_f8f6f4 v[64:67], v[200:205], v[40:45], v[64:67], v187, v187 op_sel_hi:[0,0,0] cbsz:2 blgp:2
	v_mfma_scale_f32_16x16x128_f8f6f4 v[56:59], v[206:211], v[40:45], v[56:59], v187, v187 op_sel_hi:[0,0,0] cbsz:2 blgp:2
	v_mfma_scale_f32_16x16x128_f8f6f4 v[52:55], v[46:51], v[188:193], v[52:55], v187, v187 op_sel_hi:[0,0,0] cbsz:2 blgp:2
	v_mfma_scale_f32_16x16x128_f8f6f4 v[48:51], v[194:199], v[188:193], v[224:227], v187, v187 op_sel_hi:[0,0,0] cbsz:2 blgp:2
	v_mfma_scale_f32_16x16x128_f8f6f4 v[44:47], v[200:205], v[188:193], v[212:215], v187, v187 op_sel_hi:[0,0,0] cbsz:2 blgp:2
	v_mfma_scale_f32_16x16x128_f8f6f4 v[40:43], v[206:211], v[188:193], v[216:219], v187, v187 op_sel_hi:[0,0,0] cbsz:2 blgp:2
	s_add_i32 s36, s36, 2
	s_add_u32 s11, s11, 0xc000
	s_addc_u32 s35, s35, 0
	s_add_u32 s2, s2, 0xc000
	s_addc_u32 s3, s3, 0
	s_add_u32 s72, s72, 0xc000
	s_addc_u32 s73, s73, 0
	s_cmp_lt_u32 s36, 4
	s_waitcnt lgkmcnt(0)
	s_cbranch_scc1 .LBB1_3
	s_mov_b32 s2, 1
	s_cmp_lt_i32 s2, 1
	s_cbranch_scc1 .LBB1_6

.LBB1_6:
	s_add_i32 s2, s10, 0x100
	s_cmpk_gt_i32 s10, 0xb37
	s_cselect_b64 s[10:11], -1, 0
	s_and_b64 vcc, exec, s[10:11]
	s_mov_b32 s3, s13
	s_mov_b32 s35, s34
	s_cbranch_vccnz .LBB1_1
	s_ashr_i32 s3, s2, 31
	s_lshr_b32 s3, s3, 29
	s_add_i32 s3, s2, s3
	s_ashr_i32 s35, s3, 3
	s_and_b32 s3, s3, -8
	s_sub_i32 s3, s2, s3
	s_cmp_lt_i32 s3, 0
	s_cselect_b32 s36, s12, 0x187
	s_mul_i32 s3, s36, s3
	s_add_i32 s3, s3, s35
	s_ashr_i32 s35, s3, 31
	s_lshr_b32 s35, s35, 27
	s_add_i32 s35, s3, s35
	s_ashr_i32 s36, s35, 5
	s_lshl_b32 s38, s36, 2
	s_sub_i32 s36, 0x187, s38
	s_min_u32 s39, s36, 4
	s_andn2_b32 s35, s35, 31
	s_sub_i32 s3, s3, s35
	v_cvt_f32_ubyte0_e32 v3, s39
	v_cvt_f32_i32_e32 v2, s3
	v_rcp_iflag_f32_e32 v4, v3
	s_ashr_i32 s35, s3, 30
	s_or_b32 s35, s35, 1
	v_mul_f32_e32 v4, v2, v4
	v_trunc_f32_e32 v4, v4
	v_fma_f32 v2, -v4, v3, v2
	v_cvt_i32_f32_e32 v4, v4
	v_cmp_ge_f32_e64 s[36:37], |v2|, v3
	s_and_b64 s[36:37], s[36:37], exec
	s_cselect_b32 s35, s35, 0
	v_readfirstlane_b32 s36, v4
	s_add_i32 s36, s36, s35
	s_mul_i32 s35, s36, s39
	s_sub_i32 s3, s35, s3
	s_sext_i32_i8 s3, s3
	s_sub_i32 s3, s3, s38
	s_bfe_i64 s[38:39], s[36:37], 0x80000
	s_addk_i32 s3, 0x186
	s_mul_i32 s37, s38, 0x30000
	s_mul_hi_i32 s35, s38, 0x30000
	s_add_u32 s38, s6, s37
	s_addc_u32 s39, s7, s35
	s_mul_i32 s37, s3, 0x30000
	s_mul_hi_i32 s35, s3, 0x30000
	s_add_u32 s37, s4, s37
	s_addc_u32 s35, s5, s35
	s_add_u32 s42, s38, 0x2000
	s_addc_u32 s43, s39, 0
	s_add_u32 s44, s37, 0xfffff000
	s_addc_u32 s45, s35, -1
	s_and_b64 s[40:41], s[0:1], exec
	s_cselect_b32 s41, s43, s45
	s_cselect_b32 s40, s42, s44
	s_add_u32 s42, s37, 0x1000
	s_addc_u32 s43, s35, 0
	s_mov_b64 s[44:45], s[38:39]
	s_nop 0
	s_add_u32 s40, s38, 0x3000
	s_addc_u32 s41, s39, 0
	s_add_u32 s42, s38, 0x5000
	s_addc_u32 s43, s39, 0
	s_add_u32 s44, s37, 0x2000
	s_addc_u32 s45, s35, 0
	s_and_b64 s[38:39], s[0:1], exec
	s_cselect_b32 s39, s43, s45
	s_cselect_b32 s38, s42, s44
	s_add_u32 s42, s37, 0x4000
	s_addc_u32 s43, s35, 0
	s_sext_i32_i8 s35, s36
	s_nop 0
	s_mul_i32 s68, s35, 0x30000
	s_mul_hi_i32 s69, s35, 0x30000
	s_add_u32 s68, s6, s68
	s_addc_u32 s69, s7, s69
	s_mul_i32 s70, s3, 0x30000
	s_mul_hi_i32 s71, s3, 0x30000
	s_add_u32 s70, s4, s70
	s_addc_u32 s71, s5, s71
	s_mul_i32 s67, s66, 0x3000
	s_add_u32 s68, s68, s67
	s_addc_u32 s69, s69, 0
	s_add_u32 s70, s70, s67
	s_addc_u32 s71, s71, 0
	s_cmp_eq_u32 s74, 1
	s_cselect_b32 s68, s70, s68
	s_cselect_b32 s69, s71, s69
	s_add_u32 s68, s68, s75
	s_addc_u32 s69, s69, 0
	s_mov_b32 m0, s76
	s_nop 0
	global_load_lds_dwordx4 v228, s[68:69] offset:-3072
	global_load_lds_dwordx4 v228, s[68:69] offset:-2048
	global_load_lds_dwordx4 v228, s[68:69] offset:-1024
	global_load_lds_dwordx4 v228, s[68:69]
	global_load_lds_dwordx4 v228, s[68:69] offset:1024
	global_load_lds_dwordx4 v228, s[68:69] offset:2048
	s_branch .LBB1_1

	.amdhsa_kernel _Z8knn_gemmPKcS0_Pi
		.amdhsa_group_segment_fixed_size 0
		.amdhsa_private_segment_fixed_size 0
		.amdhsa_kernarg_size 24
		.amdhsa_user_sgpr_count 2
		.amdhsa_user_sgpr_dispatch_ptr 0
		.amdhsa_user_sgpr_queue_ptr 0
		.amdhsa_user_sgpr_kernarg_segment_ptr 1
		.amdhsa_user_sgpr_dispatch_id 0
		.amdhsa_user_sgpr_kernarg_preload_length 0
		.amdhsa_user_sgpr_kernarg_preload_offset 0
		.amdhsa_user_sgpr_private_segment_size 0
		.amdhsa_uses_dynamic_stack 0
		.amdhsa_enable_private_segment 0
		.amdhsa_system_sgpr_workgroup_id_x 1
		.amdhsa_system_sgpr_workgroup_id_y 0
		.amdhsa_system_sgpr_workgroup_id_z 0
		.amdhsa_system_sgpr_workgroup_info 0
		.amdhsa_system_vgpr_workitem_id 0
		.amdhsa_next_free_vgpr 232
		.amdhsa_next_free_sgpr 78
		.amdhsa_accum_offset 232
		.amdhsa_reserve_vcc 1
		.amdhsa_float_round_mode_32 0
		.amdhsa_float_round_mode_16_64 0
		.amdhsa_float_denorm_mode_32 3
		.amdhsa_float_denorm_mode_16_64 3
		.amdhsa_dx10_clamp 1
		.amdhsa_ieee_mode 1
		.amdhsa_fp16_overflow 0
		.amdhsa_tg_split 0
		.amdhsa_exception_fp_ieee_invalid_op 0
		.amdhsa_exception_fp_denorm_src 0
		.amdhsa_exception_fp_ieee_div_zero 0
		.amdhsa_exception_fp_ieee_overflow 0
		.amdhsa_exception_fp_ieee_underflow 0
		.amdhsa_exception_fp_ieee_inexact 0
		.amdhsa_exception_int_div_zero 0
	.end_amdhsa_kernel

amdhsa.kernels:
  - .agpr_count:     0
    .args:
      - .actual_access:  read_only
        .address_space:  global
        .offset:         0
        .size:           8
        .value_kind:     global_buffer
      - .actual_access:  write_only
        .address_space:  global
        .offset:         8
        .size:           8
        .value_kind:     global_buffer
      - .actual_access:  read_only
        .address_space:  global
        .offset:         16
        .size:           8
        .value_kind:     global_buffer
      - .actual_access:  write_only
        .address_space:  global
        .offset:         24
        .size:           8
        .value_kind:     global_buffer
    .group_segment_fixed_size: 0
    .kernarg_segment_align: 8
    .kernarg_segment_size: 32
    .language:       OpenCL C
    .language_version:
      - 2
      - 0
    .max_flat_workgroup_size: 512
    .name:           _Z9prep_rowsPKfPcS0_S1_
    .private_segment_fixed_size: 0
    .sgpr_count:     28
    .sgpr_spill_count: 0
    .symbol:         _Z9prep_rowsPKfPcS0_S1_.kd
    .uniform_work_group_size: 1
    .uses_dynamic_stack: false
    .vgpr_count:     50
    .vgpr_spill_count: 0
    .wavefront_size: 64
  - .agpr_count:     0
    .args:
      - .address_space:  global
        .offset:         0
        .size:           8
        .value_kind:     global_buffer
      - .address_space:  global
        .offset:         8
        .size:           8
        .value_kind:     global_buffer
      - .actual_access:  write_only
        .address_space:  global
        .offset:         16
        .size:           8
        .value_kind:     global_buffer
    .group_segment_fixed_size: 0
    .kernarg_segment_align: 8
    .kernarg_segment_size: 24
    .language:       OpenCL C
    .language_version:
      - 2
      - 0
    .max_flat_workgroup_size: 512
    .name:           _Z8knn_gemmPKcS0_Pi
    .private_segment_fixed_size: 0
    .sgpr_count:     84
    .sgpr_spill_count: 0
    .symbol:         _Z8knn_gemmPKcS0_Pi.kd
    .uniform_work_group_size: 1
    .uses_dynamic_stack: false
    .vgpr_count:     232
    .vgpr_spill_count: 0
    .wavefront_size: 64
  - .agpr_count:     0
    .args:
      - .actual_access:  read_only
        .address_space:  global
        .offset:         0
        .size:           8
        .value_kind:     global_buffer
      - .actual_access:  read_only
        .address_space:  global
        .offset:         8
        .size:           8
        .value_kind:     global_buffer
      - .actual_access:  read_only
        .address_space:  global
        .offset:         16
        .size:           8
        .value_kind:     global_buffer
      - .actual_access:  read_only
        .address_space:  global
        .offset:         24
        .size:           8
        .value_kind:     global_buffer
      - .actual_access:  write_only
        .address_space:  global
        .offset:         32
        .size:           8
        .value_kind:     global_buffer
    .group_segment_fixed_size: 6752
    .kernarg_segment_align: 8
    .kernarg_segment_size: 40
    .language:       OpenCL C
    .language_version:
      - 2
      - 0
    .max_flat_workgroup_size: 256
    .name:           _Z10knn_selectPKiPKfS2_S2_Pf
    .private_segment_fixed_size: 0
    .sgpr_count:     42
    .sgpr_spill_count: 0
    .symbol:         _Z10knn_selectPKiPKfS2_S2_Pf.kd
    .uniform_work_group_size: 1
    .uses_dynamic_stack: false
    .vgpr_count:     124
    .vgpr_spill_count: 0
    .wavefront_size: 64
